# MoE weight-conversion loops: descriptor of the item after next evaluated too and its rows touched with eight scratch loads after the real next-item loads (two items in flight through L2; waits recount
# speedup vs baseline: 1.0041x; 1.0041x over previous
.LBB0_288:
	v_mul_u32_u24_e32 v0, s20, v66
	v_lshlrev_b32_e32 v0, 2, v0
	v_lshl_add_u64 v[2:3], s[18:19], 0, v[0:1]
	v_mul_u32_u24_e32 v0, s20, v68
	v_lshlrev_b32_e32 v0, 2, v0
	v_lshl_add_u64 v[4:5], s[18:19], 0, v[0:1]
	v_mul_u32_u24_e32 v0, s20, v70
	v_lshlrev_b32_e32 v0, 2, v0
	v_lshl_add_u64 v[10:11], s[18:19], 0, v[0:1]
	v_mul_u32_u24_e32 v0, s20, v72
	v_lshlrev_b32_e32 v0, 2, v0
	v_lshl_add_u64 v[12:13], s[18:19], 0, v[0:1]
	v_mul_u32_u24_e32 v0, s20, v67
	v_lshlrev_b32_e32 v0, 2, v0
	v_lshl_add_u64 v[18:19], s[18:19], 0, v[0:1]
	v_mul_u32_u24_e32 v0, s20, v73
	v_lshlrev_b32_e32 v0, 2, v0
	v_lshl_add_u64 v[20:21], s[18:19], 0, v[0:1]
	v_mul_u32_u24_e32 v0, s20, v80
	v_lshlrev_b32_e32 v0, 2, v0
	v_lshl_add_u64 v[26:27], s[18:19], 0, v[0:1]
	v_mul_u32_u24_e32 v0, s20, v81
	v_lshlrev_b32_e32 v0, 2, v0
	v_mov_b32_e32 v79, v1
	v_lshl_add_u64 v[28:29], s[18:19], 0, v[0:1]
	v_lshl_add_u64 v[2:3], v[2:3], 0, v[78:79]
	v_lshl_add_u64 v[4:5], v[4:5], 0, v[78:79]
	v_lshl_add_u64 v[10:11], v[10:11], 0, v[78:79]
	v_lshl_add_u64 v[12:13], v[12:13], 0, v[78:79]
	v_lshl_add_u64 v[18:19], v[18:19], 0, v[78:79]
	v_lshl_add_u64 v[20:21], v[20:21], 0, v[78:79]
	v_lshl_add_u64 v[26:27], v[26:27], 0, v[78:79]
	v_lshl_add_u64 v[28:29], v[28:29], 0, v[78:79]
	global_load_dwordx4 v[6:9], v[2:3], off nt
	s_nop 0
	global_load_dwordx4 v[2:5], v[4:5], off nt
	s_nop 0
	global_load_dwordx4 v[14:17], v[10:11], off nt
	s_nop 0
	global_load_dwordx4 v[10:13], v[12:13], off nt
	s_nop 0
	global_load_dwordx4 v[22:25], v[18:19], off nt
	s_nop 0
	global_load_dwordx4 v[18:21], v[20:21], off nt
	s_nop 0
	global_load_dwordx4 v[30:33], v[26:27], off nt
	s_nop 0
	global_load_dwordx4 v[26:29], v[28:29], off nt
	s_add_i32 s101, s40, s42
	s_cmp_gt_i32 s101, 0xa7ff
	s_cbranch_scc1 .Lpj0_none
	v_mov_b32_e32 v140, s4
	v_mov_b32_e32 v141, s5
	v_mov_b32_e32 v142, s12
	v_mov_b32_e32 v143, s13
	v_mov_b32_e32 v144, s15
	v_mov_b32_e32 v145, s18
	v_mov_b32_e32 v146, s19
	v_mov_b32_e32 v147, s20
	v_mov_b32_e32 v148, s21
	v_mov_b32_e32 v149, s22
	v_mov_b32_e32 v150, s23
	v_mov_b32_e32 v151, s48
	v_mov_b32_e32 v152, s50
	v_mov_b32_e32 v153, s52
	v_mov_b32_e32 v154, s59
	v_mov_b32_e32 v155, s62
	s_mov_b32 s40, s101
	s_add_i32 s37, s37, s65
	v_readlane_b32 s101, v254, 31
	s_add_i32 s36, s36, s101
	s_mul_hi_i32 s4, s40, 0x92492493
	s_add_i32 s4, s4, s40
	s_lshr_b32 s5, s4, 31
	s_ashr_i32 s23, s4, 10
	s_mul_hi_i32 s4, s40, 0x30c30c31
	s_add_i32 s23, s23, s5
	s_lshr_b32 s5, s4, 31
	s_ashr_i32 s4, s4, 10
	s_add_i32 s4, s4, s5
	s_mul_i32 s15, s4, -3
	s_add_i32 s15, s15, s23
	s_mov_b64 s[20:21], -1
	s_cmp_gt_i32 s15, 1
	s_mul_hi_i32 s5, s4, 0xe00000
	s_mul_i32 s22, s4, 0xe00000
	s_cbranch_scc0 .Lpj0_285
	s_and_b32 s20, s36, 0x3e0
	s_ashr_i32 s21, s4, 31
	s_add_u32 s48, s29, s22
	s_mul_i32 s12, s23, 0xfffff200
	s_addc_u32 s50, s30, s5
	s_add_i32 s12, s37, s12
	s_andn2_b32 s12, s12, 63
	s_ashr_i32 s13, s12, 31
	s_lshl_b64 s[18:19], s[12:13], 12
	s_add_u32 s18, s48, s18
	s_addc_u32 s19, s50, s19
	s_lshl_b32 s48, s20, 2
	s_add_u32 s18, s18, s48
	s_addc_u32 s19, s19, 0
	s_lshl_b32 s48, s4, 10
	s_or_b32 s20, s48, s20
	s_mul_i32 s48, s20, 0xe00
	s_mul_hi_u32 s20, s20, 0xe00
	s_mulk_i32 s21, 0xe00
	s_add_i32 s20, s20, s21
	s_add_u32 s21, s34, s48
	s_addc_u32 s20, s35, s20
	s_add_u32 s12, s21, s12
	s_addc_u32 s13, s20, s13
	s_mov_b64 s[20:21], 0

.Lpj0_288:
	v_mul_u32_u24_e32 v0, s20, v66
	v_lshlrev_b32_e32 v0, 2, v0
	v_lshl_add_u64 v[100:101], s[18:19], 0, v[0:1]
	v_mul_u32_u24_e32 v0, s20, v68
	v_lshlrev_b32_e32 v0, 2, v0
	v_lshl_add_u64 v[102:103], s[18:19], 0, v[0:1]
	v_mul_u32_u24_e32 v0, s20, v70
	v_lshlrev_b32_e32 v0, 2, v0
	v_lshl_add_u64 v[104:105], s[18:19], 0, v[0:1]
	v_mul_u32_u24_e32 v0, s20, v72
	v_lshlrev_b32_e32 v0, 2, v0
	v_lshl_add_u64 v[106:107], s[18:19], 0, v[0:1]
	v_mul_u32_u24_e32 v0, s20, v67
	v_lshlrev_b32_e32 v0, 2, v0
	v_lshl_add_u64 v[108:109], s[18:19], 0, v[0:1]
	v_mul_u32_u24_e32 v0, s20, v73
	v_lshlrev_b32_e32 v0, 2, v0
	v_lshl_add_u64 v[110:111], s[18:19], 0, v[0:1]
	v_mul_u32_u24_e32 v0, s20, v80
	v_lshlrev_b32_e32 v0, 2, v0
	v_lshl_add_u64 v[112:113], s[18:19], 0, v[0:1]
	v_mul_u32_u24_e32 v0, s20, v81
	v_lshlrev_b32_e32 v0, 2, v0
	v_mov_b32_e32 v79, v1
	v_lshl_add_u64 v[114:115], s[18:19], 0, v[0:1]
	v_lshl_add_u64 v[100:101], v[100:101], 0, v[78:79]
	v_lshl_add_u64 v[102:103], v[102:103], 0, v[78:79]
	v_lshl_add_u64 v[104:105], v[104:105], 0, v[78:79]
	v_lshl_add_u64 v[106:107], v[106:107], 0, v[78:79]
	v_lshl_add_u64 v[108:109], v[108:109], 0, v[78:79]
	v_lshl_add_u64 v[110:111], v[110:111], 0, v[78:79]
	v_lshl_add_u64 v[112:113], v[112:113], 0, v[78:79]
	v_lshl_add_u64 v[114:115], v[114:115], 0, v[78:79]
	global_load_dwordx4 v[136:139], v[100:101], off
	global_load_dwordx4 v[136:139], v[102:103], off
	global_load_dwordx4 v[136:139], v[104:105], off
	global_load_dwordx4 v[136:139], v[106:107], off
	global_load_dwordx4 v[136:139], v[108:109], off
	global_load_dwordx4 v[136:139], v[110:111], off
	global_load_dwordx4 v[136:139], v[112:113], off
	global_load_dwordx4 v[136:139], v[114:115], off
	s_sub_i32 s40, s40, s42
	s_sub_i32 s37, s37, s65
	v_readlane_b32 s101, v254, 31
	s_sub_i32 s36, s36, s101
	v_readfirstlane_b32 s4, v140
	v_readfirstlane_b32 s5, v141
	v_readfirstlane_b32 s12, v142
	v_readfirstlane_b32 s13, v143
	v_readfirstlane_b32 s15, v144
	v_readfirstlane_b32 s18, v145
	v_readfirstlane_b32 s19, v146
	v_readfirstlane_b32 s20, v147
	v_readfirstlane_b32 s21, v148
	v_readfirstlane_b32 s22, v149
	v_readfirstlane_b32 s23, v150
	v_readfirstlane_b32 s48, v151
	v_readfirstlane_b32 s50, v152
	v_readfirstlane_b32 s52, v153
	v_readfirstlane_b32 s59, v154
	v_readfirstlane_b32 s62, v155
	s_branch .Lpj0_done
.Lpj0_none:
	global_load_dwordx4 v[136:139], v1, s[18:19]
	global_load_dwordx4 v[136:139], v1, s[18:19]
	global_load_dwordx4 v[136:139], v1, s[18:19]
	global_load_dwordx4 v[136:139], v1, s[18:19]
	global_load_dwordx4 v[136:139], v1, s[18:19]
	global_load_dwordx4 v[136:139], v1, s[18:19]
	global_load_dwordx4 v[136:139], v1, s[18:19]
	global_load_dwordx4 v[136:139], v1, s[18:19]
.Lpj0_done:
	s_cmp_lg_u32 s40, s100
	s_cbranch_scc1 .LBB0_289
	s_waitcnt vmcnt(16)
	s_branch .LBB0_289

.LBB0_329:
	s_waitcnt lgkmcnt(0)
	s_andn2_b64 vcc, exec, s[16:17]
	s_mov_b64 s[10:11], -1
	s_cbranch_vccnz .LBB0_281
	v_readlane_b32 s4, v254, 31
	s_add_i32 s40, s40, s42
	s_add_i32 s37, s37, s65
	s_add_i32 s36, s36, s4
	s_mov_b64 s[10:11], 0
	s_waitcnt vmcnt(12)
	v_mov_b32_e32 v37, v29
	v_mov_b32_e32 v36, v28
	v_mov_b32_e32 v35, v27
	v_mov_b32_e32 v34, v26
	v_mov_b32_e32 v45, v33
	v_mov_b32_e32 v44, v32
	v_mov_b32_e32 v43, v31
	v_mov_b32_e32 v42, v30
	v_mov_b32_e32 v41, v21
	v_mov_b32_e32 v40, v20
	v_mov_b32_e32 v39, v19
	v_mov_b32_e32 v38, v18
	v_mov_b32_e32 v53, v25
	v_mov_b32_e32 v52, v24
	v_mov_b32_e32 v51, v23
	v_mov_b32_e32 v50, v22
	v_mov_b32_e32 v49, v13
	v_mov_b32_e32 v48, v12
	v_mov_b32_e32 v47, v11
	v_mov_b32_e32 v46, v10
	v_mov_b32_e32 v61, v17
	v_mov_b32_e32 v60, v16
	v_mov_b32_e32 v59, v15
	v_mov_b32_e32 v58, v14
	v_mov_b32_e32 v57, v5
	v_mov_b32_e32 v56, v4
	v_mov_b32_e32 v55, v3
	v_mov_b32_e32 v54, v2
	v_mov_b32_e32 v65, v9
	v_mov_b32_e32 v64, v8
	v_mov_b32_e32 v63, v7
	v_mov_b32_e32 v62, v6
	s_branch .LBB0_281

.LBB0_631:
	v_mul_u32_u24_e32 v0, s20, v66
	v_lshlrev_b32_e32 v0, 2, v0
	v_lshl_add_u64 v[2:3], s[18:19], 0, v[0:1]
	v_mul_u32_u24_e32 v0, s20, v68
	v_lshlrev_b32_e32 v0, 2, v0
	v_lshl_add_u64 v[4:5], s[18:19], 0, v[0:1]
	v_mul_u32_u24_e32 v0, s20, v70
	v_lshlrev_b32_e32 v0, 2, v0
	v_lshl_add_u64 v[10:11], s[18:19], 0, v[0:1]
	v_mul_u32_u24_e32 v0, s20, v72
	v_lshlrev_b32_e32 v0, 2, v0
	v_lshl_add_u64 v[12:13], s[18:19], 0, v[0:1]
	v_mul_u32_u24_e32 v0, s20, v67
	v_lshlrev_b32_e32 v0, 2, v0
	v_lshl_add_u64 v[18:19], s[18:19], 0, v[0:1]
	v_mul_u32_u24_e32 v0, s20, v73
	v_lshlrev_b32_e32 v0, 2, v0
	v_lshl_add_u64 v[20:21], s[18:19], 0, v[0:1]
	v_mul_u32_u24_e32 v0, s20, v80
	v_lshlrev_b32_e32 v0, 2, v0
	v_lshl_add_u64 v[26:27], s[18:19], 0, v[0:1]
	v_mul_u32_u24_e32 v0, s20, v81
	v_lshlrev_b32_e32 v0, 2, v0
	v_mov_b32_e32 v79, v1
	v_lshl_add_u64 v[28:29], s[18:19], 0, v[0:1]
	v_lshl_add_u64 v[2:3], v[2:3], 0, v[78:79]
	v_lshl_add_u64 v[4:5], v[4:5], 0, v[78:79]
	v_lshl_add_u64 v[10:11], v[10:11], 0, v[78:79]
	v_lshl_add_u64 v[12:13], v[12:13], 0, v[78:79]
	v_lshl_add_u64 v[18:19], v[18:19], 0, v[78:79]
	v_lshl_add_u64 v[20:21], v[20:21], 0, v[78:79]
	v_lshl_add_u64 v[26:27], v[26:27], 0, v[78:79]
	v_lshl_add_u64 v[28:29], v[28:29], 0, v[78:79]
	global_load_dwordx4 v[6:9], v[2:3], off nt
	s_nop 0
	global_load_dwordx4 v[2:5], v[4:5], off nt
	s_nop 0
	global_load_dwordx4 v[14:17], v[10:11], off nt
	s_nop 0
	global_load_dwordx4 v[10:13], v[12:13], off nt
	s_nop 0
	global_load_dwordx4 v[22:25], v[18:19], off nt
	s_nop 0
	global_load_dwordx4 v[18:21], v[20:21], off nt
	s_nop 0
	global_load_dwordx4 v[30:33], v[26:27], off nt
	s_nop 0
	global_load_dwordx4 v[26:29], v[28:29], off nt
	s_add_i32 s101, s37, s42
	s_cmp_gt_i32 s101, 0xa7ff
	s_cbranch_scc1 .Lpj2_none
	v_mov_b32_e32 v140, s4
	v_mov_b32_e32 v141, s5
	v_mov_b32_e32 v142, s12
	v_mov_b32_e32 v143, s13
	v_mov_b32_e32 v144, s15
	v_mov_b32_e32 v145, s18
	v_mov_b32_e32 v146, s19
	v_mov_b32_e32 v147, s20
	v_mov_b32_e32 v148, s21
	v_mov_b32_e32 v149, s22
	v_mov_b32_e32 v150, s23
	v_mov_b32_e32 v151, s40
	v_mov_b32_e32 v152, s41
	v_mov_b32_e32 v153, s44
	s_mov_b32 s37, s101
	s_add_i32 s36, s36, s65
	v_readlane_b32 s101, v254, 31
	s_add_i32 s35, s35, s101
	s_mul_hi_i32 s4, s37, 0x92492493
	s_add_i32 s4, s4, s37
	s_lshr_b32 s5, s4, 31
	s_ashr_i32 s23, s4, 10
	s_mul_hi_i32 s4, s37, 0x30c30c31
	s_add_i32 s23, s23, s5
	s_lshr_b32 s5, s4, 31
	s_ashr_i32 s4, s4, 10
	s_add_i32 s4, s4, s5
	s_mul_i32 s15, s4, -3
	s_add_i32 s15, s15, s23
	s_mov_b64 s[20:21], -1
	s_cmp_gt_i32 s15, 1
	s_mul_hi_i32 s5, s4, 0xe00000
	s_mul_i32 s22, s4, 0xe00000
	s_cbranch_scc0 .Lpj2_628
	s_and_b32 s20, s35, 0x3e0
	s_ashr_i32 s21, s4, 31
	s_add_u32 s40, s28, s22
	s_mul_i32 s12, s23, 0xfffff200
	s_addc_u32 s41, s29, s5
	s_add_i32 s12, s36, s12
	s_andn2_b32 s12, s12, 63
	s_ashr_i32 s13, s12, 31
	s_lshl_b64 s[18:19], s[12:13], 12
	s_add_u32 s18, s40, s18
	s_addc_u32 s19, s41, s19
	s_lshl_b32 s40, s20, 2
	s_add_u32 s18, s18, s40
	s_addc_u32 s19, s19, 0
	s_lshl_b32 s40, s4, 10
	s_or_b32 s20, s40, s20
	s_mul_i32 s40, s20, 0xe00
	s_mul_hi_u32 s20, s20, 0xe00
	s_mulk_i32 s21, 0xe00
	s_add_i32 s20, s20, s21
	s_add_u32 s21, s33, s40
	s_addc_u32 s20, s34, s20
	s_add_u32 s12, s21, s12
	s_addc_u32 s13, s20, s13
	s_mov_b64 s[20:21], 0

.Lpj2_631:
	v_mul_u32_u24_e32 v0, s20, v66
	v_lshlrev_b32_e32 v0, 2, v0
	v_lshl_add_u64 v[100:101], s[18:19], 0, v[0:1]
	v_mul_u32_u24_e32 v0, s20, v68
	v_lshlrev_b32_e32 v0, 2, v0
	v_lshl_add_u64 v[102:103], s[18:19], 0, v[0:1]
	v_mul_u32_u24_e32 v0, s20, v70
	v_lshlrev_b32_e32 v0, 2, v0
	v_lshl_add_u64 v[104:105], s[18:19], 0, v[0:1]
	v_mul_u32_u24_e32 v0, s20, v72
	v_lshlrev_b32_e32 v0, 2, v0
	v_lshl_add_u64 v[106:107], s[18:19], 0, v[0:1]
	v_mul_u32_u24_e32 v0, s20, v67
	v_lshlrev_b32_e32 v0, 2, v0
	v_lshl_add_u64 v[108:109], s[18:19], 0, v[0:1]
	v_mul_u32_u24_e32 v0, s20, v73
	v_lshlrev_b32_e32 v0, 2, v0
	v_lshl_add_u64 v[110:111], s[18:19], 0, v[0:1]
	v_mul_u32_u24_e32 v0, s20, v80
	v_lshlrev_b32_e32 v0, 2, v0
	v_lshl_add_u64 v[112:113], s[18:19], 0, v[0:1]
	v_mul_u32_u24_e32 v0, s20, v81
	v_lshlrev_b32_e32 v0, 2, v0
	v_mov_b32_e32 v79, v1
	v_lshl_add_u64 v[114:115], s[18:19], 0, v[0:1]
	v_lshl_add_u64 v[100:101], v[100:101], 0, v[78:79]
	v_lshl_add_u64 v[102:103], v[102:103], 0, v[78:79]
	v_lshl_add_u64 v[104:105], v[104:105], 0, v[78:79]
	v_lshl_add_u64 v[106:107], v[106:107], 0, v[78:79]
	v_lshl_add_u64 v[108:109], v[108:109], 0, v[78:79]
	v_lshl_add_u64 v[110:111], v[110:111], 0, v[78:79]
	v_lshl_add_u64 v[112:113], v[112:113], 0, v[78:79]
	v_lshl_add_u64 v[114:115], v[114:115], 0, v[78:79]
	global_load_dwordx4 v[136:139], v[100:101], off
	global_load_dwordx4 v[136:139], v[102:103], off
	global_load_dwordx4 v[136:139], v[104:105], off
	global_load_dwordx4 v[136:139], v[106:107], off
	global_load_dwordx4 v[136:139], v[108:109], off
	global_load_dwordx4 v[136:139], v[110:111], off
	global_load_dwordx4 v[136:139], v[112:113], off
	global_load_dwordx4 v[136:139], v[114:115], off
	s_sub_i32 s37, s37, s42
	s_sub_i32 s36, s36, s65
	v_readlane_b32 s101, v254, 31
	s_sub_i32 s35, s35, s101
	v_readfirstlane_b32 s4, v140
	v_readfirstlane_b32 s5, v141
	v_readfirstlane_b32 s12, v142
	v_readfirstlane_b32 s13, v143
	v_readfirstlane_b32 s15, v144
	v_readfirstlane_b32 s18, v145
	v_readfirstlane_b32 s19, v146
	v_readfirstlane_b32 s20, v147
	v_readfirstlane_b32 s21, v148
	v_readfirstlane_b32 s22, v149
	v_readfirstlane_b32 s23, v150
	v_readfirstlane_b32 s40, v151
	v_readfirstlane_b32 s41, v152
	v_readfirstlane_b32 s44, v153
	s_branch .Lpj2_done

.Lpj2_done:
	s_cmp_lg_u32 s37, s100
	s_cbranch_scc1 .LBB0_632
	s_waitcnt vmcnt(16)
	s_branch .LBB0_632

.LBB0_672:
	s_waitcnt lgkmcnt(0)
	s_andn2_b64 vcc, exec, s[16:17]
	s_mov_b64 s[10:11], -1
	s_cbranch_vccnz .LBB0_624
	v_readlane_b32 s4, v254, 31
	s_add_i32 s37, s37, s42
	s_add_i32 s36, s36, s65
	s_add_i32 s35, s35, s4
	s_mov_b64 s[10:11], 0
	s_waitcnt vmcnt(12)
	v_mov_b32_e32 v37, v29
	v_mov_b32_e32 v36, v28
	v_mov_b32_e32 v35, v27
	v_mov_b32_e32 v34, v26
	v_mov_b32_e32 v45, v33
	v_mov_b32_e32 v44, v32
	v_mov_b32_e32 v43, v31
	v_mov_b32_e32 v42, v30
	v_mov_b32_e32 v41, v21
	v_mov_b32_e32 v40, v20
	v_mov_b32_e32 v39, v19
	v_mov_b32_e32 v38, v18
	v_mov_b32_e32 v53, v25
	v_mov_b32_e32 v52, v24
	v_mov_b32_e32 v51, v23
	v_mov_b32_e32 v50, v22
	v_mov_b32_e32 v49, v13
	v_mov_b32_e32 v48, v12
	v_mov_b32_e32 v47, v11
	v_mov_b32_e32 v46, v10
	v_mov_b32_e32 v61, v17
	v_mov_b32_e32 v60, v16
	v_mov_b32_e32 v59, v15
	v_mov_b32_e32 v58, v14
	v_mov_b32_e32 v57, v5
	v_mov_b32_e32 v56, v4
	v_mov_b32_e32 v55, v3
	v_mov_b32_e32 v54, v2
	v_mov_b32_e32 v65, v9
	v_mov_b32_e32 v64, v8
	v_mov_b32_e32 v63, v7
	v_mov_b32_e32 v62, v6
	s_branch .LBB0_624
